# speedup vs baseline: 1.0143x; 1.0143x over previous
.LBB3_17:
	s_and_b64 vcc, exec, s[2:3]
	s_cbranch_vccz .LBB3_27
	s_load_dwordx2 s[8:9], s[0:1], 0x70
	s_load_dwordx4 s[4:7], s[0:1], 0x40
	s_load_dwordx4 s[20:23], s[0:1], 0x10
	s_load_dwordx4 s[28:31], s[0:1], 0x20
	s_load_dwordx4 s[32:35], s[0:1], 0x30
	s_load_dwordx2 s[36:37], s[0:1], 0x60
	v_mov_b32_e32 v3, 0
	v_lshlrev_b32_e32 v2, 2, v0
	s_movk_i32 s2, 0xfe00
	s_mov_b32 s3, -1
	s_waitcnt lgkmcnt(0)
	v_lshl_add_u64 v[6:7], s[22:23], 0, v[2:3]
	s_lshr_b32 s16, s15, 7
	s_movk_i32 s10, 0x80
	v_lshl_add_u64 v[6:7], v[6:7], 0, s[2:3]
	s_lshl_b32 s2, s12, 3
	v_cmp_gt_u32_e32 vcc, s10, v0
	s_or_b32 s10, s16, s2
	v_lshl_add_u64 v[4:5], s[20:21], 0, v[2:3]
	s_ashr_i32 s11, s10, 31
	v_cndmask_b32_e32 v6, v6, v4, vcc
	s_movk_i32 s17, 0x1000
	s_bfe_u32 s13, s15, 0x10006
	s_lshl_b64 s[2:3], s[10:11], 12
	v_and_b32_e32 v156, 63, v0
	v_cndmask_b32_e32 v7, v7, v5, vcc
	v_add_co_u32_e32 v20, vcc, s17, v6
	s_add_u32 s2, s8, s2
	s_nop 0
	v_addc_co_u32_e32 v21, vcc, 0, v7, vcc
	s_addc_u32 s3, s9, s3
	v_lshlrev_b32_e32 v1, 3, v156
	global_load_dword v17, v[6:7], off
	global_load_dword v16, v[6:7], off offset:512
	global_load_dword v13, v[6:7], off offset:1024
	global_load_dword v12, v[6:7], off offset:1536
	global_load_dword v9, v[6:7], off offset:2048
	global_load_dword v8, v[6:7], off offset:2560
	global_load_dword v5, v[6:7], off offset:3072
	global_load_dword v4, v[6:7], off offset:3584
	global_load_dword v19, v[20:21], off
	global_load_dword v18, v[20:21], off offset:512
	global_load_dword v15, v[20:21], off offset:1024
	global_load_dword v14, v[20:21], off offset:1536
	global_load_dword v11, v[20:21], off offset:2048
	global_load_dword v10, v[20:21], off offset:2560
	global_load_dword v7, v[20:21], off offset:3072
	global_load_dword v6, v[20:21], off offset:3584
	s_cmpk_lt_u32 s15, 0x80
	s_cselect_b32 s38, s28, s32
	s_cselect_b32 s39, s29, s33
	s_cselect_b32 s40, s30, s34
	s_cselect_b32 s41, s31, s35
	v_and_b32_e32 v24, 0x1fc, v2
	v_and_b32_e32 v28, 0xfc, v2
	v_lshl_or_b32 v28, s14, 8, v28
	global_load_dword v25, v24, s[38:39]
	global_load_dword v26, v24, s[40:41]
	global_load_dword v27, v28, s[36:37]
	global_load_dwordx2 v[154:155], v1, s[2:3]
	global_load_dwordx2 v[150:151], v1, s[2:3] offset:512
	global_load_dwordx2 v[146:147], v1, s[2:3] offset:1024
	global_load_dwordx2 v[142:143], v1, s[2:3] offset:1536
	global_load_dwordx2 v[152:153], v1, s[2:3] offset:2048
	global_load_dwordx2 v[148:149], v1, s[2:3] offset:2560
	global_load_dwordx2 v[144:145], v1, s[2:3] offset:3072
	global_load_dwordx2 v[140:141], v1, s[2:3] offset:3584
	s_lshl_b32 s2, s14, 10
	s_lshl_b32 s3, s13, 9
	s_or_b32 s2, s3, s2
	v_or_b32_e32 v1, s2, v156
	v_lshlrev_b32_e32 v20, 4, v1
	v_mov_b32_e32 v21, v3
	v_lshl_add_u64 v[22:23], s[4:5], 0, v[20:21]
	v_add_co_u32_e32 v22, vcc, s17, v22
	s_movk_i32 s2, 0x7f
	s_nop 0
	v_addc_co_u32_e32 v23, vcc, 0, v23, vcc
	global_load_dwordx4 v[86:89], v[22:23], off
	global_load_dwordx4 v[78:81], v[22:23], off offset:1024
	global_load_dwordx4 v[70:73], v[22:23], off offset:2048
	global_load_dwordx4 v[66:69], v[22:23], off offset:3072
	global_load_dwordx4 v[122:125], v20, s[4:5]
	global_load_dwordx4 v[126:129], v20, s[6:7]
	global_load_dwordx4 v[114:117], v20, s[4:5] offset:1024
	global_load_dwordx4 v[118:121], v20, s[6:7] offset:1024
	global_load_dwordx4 v[106:109], v20, s[4:5] offset:2048
	global_load_dwordx4 v[110:113], v20, s[6:7] offset:2048
	global_load_dwordx4 v[98:101], v20, s[4:5] offset:3072
	global_load_dwordx4 v[102:105], v20, s[6:7] offset:3072
	v_lshl_add_u64 v[22:23], s[6:7], 0, v[20:21]
	v_add_co_u32_e32 v20, vcc, 0x1000, v22
	s_nop 1
	v_addc_co_u32_e32 v21, vcc, 0, v23, vcc
	global_load_dwordx4 v[94:97], v[20:21], off
	global_load_dwordx4 v[90:93], v[20:21], off offset:1024
	global_load_dwordx4 v[82:85], v[20:21], off offset:2048
	global_load_dwordx4 v[74:77], v[20:21], off offset:3072
	v_cmp_lt_u32_e32 vcc, s2, v0
	v_cmp_gt_u32_e64 s[2:3], 64, v0
	s_and_saveexec_b64 s[4:5], s[2:3]
	s_cbranch_execz .LBB3_20
	v_add_u32_e32 v20, 0x1ee00, v2
	s_waitcnt vmcnt(24)
	ds_write_b32 v20, v27
.LBB3_20:
	s_or_b64 exec, exec, s[4:5]
	s_waitcnt vmcnt(41)
	v_pk_add_f32 v[16:17], v[16:17], 0 op_sel_hi:[1,0]
	s_waitcnt vmcnt(39)
	v_pk_add_f32 v[12:13], v[16:17], v[12:13]
	s_waitcnt vmcnt(37)
	v_pk_add_f32 v[8:9], v[12:13], v[8:9]
	s_waitcnt vmcnt(35)
	v_pk_add_f32 v[4:5], v[8:9], v[4:5]
	s_waitcnt vmcnt(33)
	v_pk_add_f32 v[4:5], v[4:5], v[18:19]
	s_waitcnt vmcnt(31)
	v_pk_add_f32 v[4:5], v[4:5], v[14:15]
	s_waitcnt vmcnt(29)
	v_pk_add_f32 v[4:5], v[4:5], v[10:11]
	s_waitcnt vmcnt(27)
	v_pk_add_f32 v[4:5], v[4:5], v[6:7]
	s_and_saveexec_b64 s[2:3], vcc
	s_xor_b64 s[2:3], exec, s[2:3]
	s_cbranch_execz .LBB3_22
	v_add_u32_e32 v2, 0xffffff80, v0
	v_lshlrev_b32_e32 v2, 2, v2
	s_mov_b32 s4, 0x39000000
	v_pk_mul_f32 v[4:5], v[4:5], s[4:5] op_sel_hi:[1,0]
	v_add_u32_e32 v6, 0x1e800, v2
	v_fma_f32 v4, -v5, v5, v4
	v_max_f32_e32 v4, 0, v4
	v_add_f32_e32 v4, 0x3727c5ac, v4
	v_rsq_f32_e32 v4, v4
	s_waitcnt vmcnt(26)
	v_mul_f32_e32 v1, v4, v25
	s_waitcnt vmcnt(25)
	v_fma_f32 v3, -v5, v1, v26
	ds_write_b32 v6, v1
	v_add_u32_e32 v1, 0x1ec00, v2
	ds_write_b32 v1, v3
.LBB3_22:
	s_andn2_saveexec_b64 s[2:3], s[2:3]
	s_cbranch_execz .LBB3_24
	s_mov_b32 s0, 0x37800000
	v_pk_mul_f32 v[4:5], v[4:5], s[0:1] op_sel_hi:[1,0]
	v_fma_f32 v4, -v5, v5, v4
	v_max_f32_e32 v4, 0, v4
	v_add_f32_e32 v4, 0x3727c5ac, v4
	v_rsq_f32_e32 v4, v4
	v_add_u32_e32 v6, 0x1e600, v2
	v_add_u32_e32 v7, 0x1ea00, v2
	v_add_u32_e32 v2, 0x1e400, v2
	v_mov_b32_e32 v8, 0
	s_waitcnt vmcnt(26)
	v_mul_f32_e32 v1, v4, v25
	s_waitcnt vmcnt(25)
	v_fma_f32 v3, -v5, v1, v26
	ds_write_b32 v6, v1
	ds_write_b32 v7, v3
	ds_write_b32 v2, v8
